# GLA phase A: q/k row loads issued at the unit top with the decay loads (one round trip less per unit); gla_c: LDS-shared state tile by DMA, all unit loads issued up front; earlier layout changes
# speedup vs baseline: 1.0225x; 1.0132x over previous
.LBB0_818:
	s_and_b32 s91, s85, 3
	s_ashr_i32 s43, s43, 7
	s_add_i32 s82, s43, s76
	s_mul_i32 s43, s84, 0x900
	s_lshl_b32 s89, s91, 8
	s_add_i32 s43, s43, s89
	s_add_i32 s76, s43, 0x400
	s_ashr_i32 s43, s42, 31
	v_lshl_add_u64 v[0:1], v[58:59], 0, s[76:77]
	v_lshl_add_u64 v[2:3], s[42:43], 1, v[60:61]
	v_mad_u64_u32 v[2:3], s[42:43], v0, s75, v[2:3]
	v_mov_b32_e32 v0, v3
	v_mad_u64_u32 v[0:1], s[42:43], v1, s75, v[0:1]
	v_mov_b32_e32 v3, v0
	s_mov_b32 s42, 0x12000
	s_barrier
	global_load_dwordx4 v[44:47], v[2:3], off
	global_load_dwordx4 v[40:43], v[2:3], off offset:64
	v_add_co_u32_e32 v2, vcc, s42, v2
	s_mul_hi_i32 s42, s82, 0x2400
	s_mulk_i32 s82, 0x2400
	s_add_u32 s82, s82, s90
	s_addc_u32 s83, s42, 0
	v_addc_co_u32_e32 v3, vcc, 0, v0, vcc
	v_lshl_add_u64 v[0:1], s[82:83], 0, v[62:63]
	s_lshl_b32 s76, s91, 9
	global_load_dwordx4 v[36:39], v[2:3], off
	global_load_dwordx4 v[32:35], v[2:3], off offset:64
	v_lshl_add_u64 v[2:3], v[64:65], 0, s[76:77]
	v_lshlrev_b64 v[0:1], 11, v[0:1]
	v_lshl_add_u64 v[0:1], v[2:3], 0, v[0:1]
	v_add_co_u32_e32 v2, vcc, s57, v0
	s_add_i32 s76, s92, 0x23f
	s_nop 0
	v_addc_co_u32_e32 v3, vcc, 0, v1, vcc
	v_add_co_u32_e32 v4, vcc, s53, v0
	s_cmpk_lt_u32 s76, 0x47f
	s_nop 0
	v_addc_co_u32_e32 v5, vcc, 0, v1, vcc
	v_add_co_u32_e32 v6, vcc, s70, v0
	s_cselect_b64 s[42:43], -1, 0
	s_nop 0
	v_addc_co_u32_e32 v7, vcc, 0, v1, vcc
	v_add_co_u32_e32 v8, vcc, s62, v0
	s_cmpk_gt_u32 s76, 0x47e
	s_nop 0
	v_addc_co_u32_e32 v9, vcc, 0, v1, vcc
	v_add_co_u32_e32 v10, vcc, s61, v0
	s_cselect_b64 s[84:85], -1, 0
	s_nop 0
	v_addc_co_u32_e32 v11, vcc, 0, v1, vcc
	v_add_co_u32_e32 v12, vcc, s63, v0
	s_mov_b64 s[86:87], -1
	s_nop 0
	v_addc_co_u32_e32 v13, vcc, 0, v1, vcc
	global_load_dword v18, v[4:5], off offset:-4096
	global_load_dword v20, v[4:5], off
	global_load_dword v21, v[4:5], off offset:2048
	global_load_dword v22, v[8:9], off offset:-4096
	global_load_dword v24, v[8:9], off
	global_load_dword v25, v[8:9], off offset:2048
	global_load_dword v26, v[12:13], off offset:-4096
	global_load_dword v28, v[12:13], off
	global_load_dword v29, v[12:13], off offset:2048
	v_add_co_u32_e32 v4, vcc, 0x7000, v0
	s_nop 1
	v_addc_co_u32_e32 v5, vcc, 0, v1, vcc
	global_load_dword v16, v[0:1], off
	global_load_dword v17, v[0:1], off offset:2048
	global_load_dword v19, v[2:3], off offset:2048
	global_load_dword v23, v[6:7], off offset:2048
	global_load_dword v27, v[10:11], off offset:2048
	global_load_dword v30, v[4:5], off
	global_load_dword v31, v[4:5], off offset:2048
	v_add_u32_e32 v114, s90, v66
	v_mov_b64_e32 v[116:117], s[78:79]
	v_mad_i64_i32 v[116:117], vcc, v114, s59, v[116:117]
	s_lshl_b32 s76, s91, 8
	v_lshl_add_u64 v[116:117], v[116:117], 0, s[76:77]
	v_lshl_add_u64 v[116:117], v[116:117], 0, v[96:97]
	s_movk_i32 s76, 0x1800
	v_lshl_add_u64 v[116:117], v[116:117], 0, s[76:77]
	global_load_dwordx4 v[120:123], v[116:117], off
	global_load_dwordx4 v[124:127], v[116:117], off offset:16
	global_load_dwordx4 v[128:131], v[116:117], off offset:1024
	global_load_dwordx4 v[132:135], v[116:117], off offset:1040
	s_and_b64 vcc, exec, s[42:43]
	s_cbranch_vccnz .LBB0_820
	s_waitcnt vmcnt(0)
	v_add_f32_e32 v49, v30, v31
	v_add_f32_e32 v50, v29, v49
	v_add_f32_e32 v51, v28, v50
	v_add_f32_e32 v52, v27, v51
	v_add_f32_e32 v53, v26, v52
	v_add_f32_e32 v54, v25, v53
	v_add_f32_e32 v55, v24, v54
	v_add_f32_e32 v106, v23, v55
	v_add_f32_e32 v107, v22, v106
	v_add_f32_e32 v108, v21, v107
	v_add_f32_e32 v109, v20, v108
	v_add_f32_e32 v110, v19, v109
	v_add_f32_e32 v111, v18, v110
	v_add_f32_e32 v112, v17, v111
	v_mov_b64_e32 v[0:1], v[16:17]
	v_add_f32_e32 v48, v16, v112
	v_mov_b64_e32 v[2:3], v[18:19]
	v_mov_b64_e32 v[4:5], v[20:21]
	v_mov_b64_e32 v[6:7], v[22:23]
	v_mov_b64_e32 v[8:9], v[24:25]
	v_mov_b64_e32 v[10:11], v[26:27]
	v_mov_b64_e32 v[12:13], v[28:29]
	v_mov_b64_e32 v[14:15], v[30:31]
	v_mov_b32_e32 v0, v48
	v_mov_b32_e32 v1, v112
	v_mov_b32_e32 v2, v111
	v_mov_b32_e32 v3, v110
	v_mov_b32_e32 v4, v109
	v_mov_b32_e32 v5, v108
	v_mov_b32_e32 v6, v107
	v_mov_b32_e32 v7, v106
	v_mov_b32_e32 v8, v55
	v_mov_b32_e32 v9, v54
	v_mov_b32_e32 v10, v53
	v_mov_b32_e32 v11, v52
	v_mov_b32_e32 v12, v51
	v_mov_b32_e32 v13, v50
	v_mov_b32_e32 v14, v49
	s_mov_b64 s[86:87], 0

.LBB0_834:
	s_waitcnt vmcnt(6)
	v_add_f32_e32 v0, v0, v16
	v_add_f32_e32 v1, v1, v16
	ds_write2st64_b32 v93, v0, v1 offset1:2
	v_add_f32_e32 v0, v2, v16
	v_add_f32_e32 v1, v3, v16
	ds_write2st64_b32 v93, v0, v1 offset0:4 offset1:6
	v_add_f32_e32 v0, v4, v16
	v_add_f32_e32 v1, v5, v16
	ds_write2st64_b32 v93, v0, v1 offset0:8 offset1:10
	v_add_f32_e32 v0, v6, v16
	v_add_f32_e32 v1, v7, v16
	ds_write2st64_b32 v93, v0, v1 offset0:12 offset1:14
	v_add_f32_e32 v0, v8, v16
	v_add_f32_e32 v1, v9, v16
	ds_write2st64_b32 v93, v0, v1 offset0:16 offset1:18
	v_add_f32_e32 v0, v10, v16
	v_add_f32_e32 v1, v11, v16
	ds_write2st64_b32 v93, v0, v1 offset0:20 offset1:22
	v_add_f32_e32 v0, v12, v16
	v_add_f32_e32 v1, v13, v16
	ds_write2st64_b32 v93, v0, v1 offset0:24 offset1:26
	v_add_f32_e32 v0, v14, v16
	v_add_f32_e32 v1, v15, v16
	ds_write2st64_b32 v93, v0, v1 offset0:28 offset1:30
	v_add_u32_e32 v2, s90, v66
	v_mov_b64_e32 v[0:1], s[78:79]
	v_mad_i64_i32 v[0:1], s[84:85], v2, s59, v[0:1]
	s_lshl_b32 s76, s76, 1
	v_lshl_add_u64 v[0:1], v[0:1], 0, s[76:77]
	v_lshl_add_u64 v[4:5], v[0:1], 0, v[96:97]
	s_mov_b64 s[84:85], 0x1800
	v_add_co_u32_e32 v6, vcc, s57, v4
	v_lshl_add_u64 v[0:1], v[4:5], 0, s[84:85]
	s_nop 0
	v_addc_co_u32_e32 v7, vcc, 0, v5, vcc
	s_waitcnt lgkmcnt(0)
	s_barrier
	s_nop 0
	s_mov_b64 s[84:85], 0x1c00
	v_lshl_add_u64 v[4:5], v[4:5], 0, s[84:85]
	s_nop 0
	ds_read_b128 v[48:51], v98
	s_waitcnt vmcnt(6)
	ds_read_b128 v[24:27], v98 offset:16
	ds_read_b128 v[16:19], v98 offset:32
	v_add_u32_e32 v106, s86, v95
	ds_read_b128 v[52:55], v106
	s_waitcnt vmcnt(4)
	ds_read_b128 v[28:31], v106 offset:16
	ds_read_b128 v[20:23], v106 offset:32
	s_waitcnt lgkmcnt(5)
	v_mul_f32_e32 v107, 0x3fb8aa3b, v48
	v_exp_f32_e32 v108, v107
	v_mul_f32_e32 v107, 0xbfb8aa3b, v48
	s_waitcnt lgkmcnt(2)
	v_sub_f32_e32 v48, v52, v48
	v_mul_f32_e32 v52, 0x3fb8aa3b, v49
	v_mul_f32_e32 v48, 0x3fb8aa3b, v48
	v_exp_f32_e32 v109, v52
	v_exp_f32_e32 v48, v48
	v_exp_f32_e32 v110, v107
	s_ashr_i32 s93, s92, 31
	s_waitcnt vmcnt(3)
	v_lshlrev_b32_e32 v112, 16, v120
	v_and_b32_e32 v113, 0xffff0000, v120
	v_pk_mul_f32 v[112:113], v[112:113], s[50:51] op_sel_hi:[1,0]
	v_mul_f32_e32 v8, 0xbfb8aa3b, v49
	v_pk_mul_f32 v[108:109], v[112:113], v[108:109]
	s_waitcnt vmcnt(1)
	v_lshlrev_b32_e32 v112, 16, v128
	v_exp_f32_e32 v111, v8
	v_mul_f32_e32 v8, v48, v112
	v_and_b32_e32 v113, 0xffff0000, v128
	v_bfe_u32 v12, v8, 16, 1
	v_add3_u32 v8, v8, v12, s51
	ds_write_b16_d16_hi v101, v8
	v_sub_f32_e32 v8, v53, v49
	v_mul_f32_e32 v8, 0x3fb8aa3b, v8
	v_exp_f32_e32 v8, v8
	v_mul_f32_e32 v49, 0xbfb8aa3b, v50
	v_exp_f32_e32 v52, v49
	v_sub_f32_e32 v49, v54, v50
	v_mul_f32_e32 v49, 0x3fb8aa3b, v49
	v_mul_f32_e32 v8, v8, v113
	v_mul_f32_e32 v48, 0x3fb8aa3b, v50
	v_exp_f32_e32 v50, v49
	v_mul_f32_e32 v49, 0x3fb8aa3b, v51
	v_bfe_u32 v12, v8, 16, 1
	v_exp_f32_e32 v48, v48
	v_exp_f32_e32 v49, v49
	v_add3_u32 v8, v8, v12, s51
	ds_write_b16_d16_hi v101, v8 offset:144
	v_cvt_pk_bf16_f32 v8, v108, v109
	v_lshlrev_b32_e32 v108, 16, v121
	v_and_b32_e32 v109, 0xffff0000, v121
	v_pk_mul_f32 v[108:109], v[108:109], s[50:51] op_sel_hi:[1,0]
	v_mul_f32_e32 v9, 0xbfb8aa3b, v51
	v_pk_mul_f32 v[48:49], v[108:109], v[48:49]
	v_lshlrev_b32_e32 v108, 16, v129
	v_exp_f32_e32 v53, v9
	v_mul_f32_e32 v9, v50, v108
	v_and_b32_e32 v109, 0xffff0000, v129
	v_bfe_u32 v13, v9, 16, 1
	v_add3_u32 v9, v9, v13, s51
	ds_write_b16_d16_hi v101, v9 offset:288
	v_sub_f32_e32 v9, v55, v51
	v_mul_f32_e32 v9, 0x3fb8aa3b, v9
	v_exp_f32_e32 v9, v9
	v_pk_mul_f32 v[52:53], v[52:53], v[108:109]
	v_pk_mul_f32 v[110:111], v[110:111], v[112:113]
	v_mul_f32_e32 v9, v9, v109
	v_bfe_u32 v13, v9, 16, 1
	v_add3_u32 v9, v9, v13, s51
	ds_write_b16_d16_hi v101, v9 offset:432
	v_cvt_pk_bf16_f32 v9, v48, v49
	v_mul_f32_e32 v48, 0x3fb8aa3b, v24
	v_mul_f32_e32 v49, 0xbfb8aa3b, v24
	s_waitcnt lgkmcnt(5)
	v_sub_f32_e32 v24, v28, v24
	v_mul_f32_e32 v28, 0x3fb8aa3b, v25
	v_exp_f32_e32 v48, v48
	v_exp_f32_e32 v50, v49
	v_mul_f32_e32 v24, 0x3fb8aa3b, v24
	v_exp_f32_e32 v49, v28
	v_exp_f32_e32 v24, v24
	v_cvt_pk_bf16_f32 v13, v52, v53
	v_lshlrev_b32_e32 v52, 16, v122
	v_and_b32_e32 v53, 0xffff0000, v122
	v_pk_mul_f32 v[52:53], v[52:53], s[50:51] op_sel_hi:[1,0]
	v_mul_f32_e32 v10, 0xbfb8aa3b, v25
	v_pk_mul_f32 v[48:49], v[52:53], v[48:49]
	v_lshlrev_b32_e32 v52, 16, v130
	v_exp_f32_e32 v51, v10
	v_mul_f32_e32 v10, v24, v52
	v_and_b32_e32 v53, 0xffff0000, v130
	v_bfe_u32 v14, v10, 16, 1
	v_add3_u32 v10, v10, v14, s51
	ds_write_b16_d16_hi v101, v10 offset:576
	v_sub_f32_e32 v10, v29, v25
	v_mul_f32_e32 v10, 0x3fb8aa3b, v10
	v_exp_f32_e32 v10, v10
	v_mul_f32_e32 v25, 0xbfb8aa3b, v26
	v_exp_f32_e32 v28, v25
	v_sub_f32_e32 v25, v30, v26
	v_mul_f32_e32 v25, 0x3fb8aa3b, v25
	v_mul_f32_e32 v10, v10, v53
	v_mul_f32_e32 v24, 0x3fb8aa3b, v26
	v_exp_f32_e32 v26, v25
	v_mul_f32_e32 v25, 0x3fb8aa3b, v27
	v_bfe_u32 v14, v10, 16, 1
	v_exp_f32_e32 v24, v24
	v_exp_f32_e32 v25, v25
	v_add3_u32 v10, v10, v14, s51
	ds_write_b16_d16_hi v101, v10 offset:720
	v_cvt_pk_bf16_f32 v10, v48, v49
	v_lshlrev_b32_e32 v48, 16, v123
	v_and_b32_e32 v49, 0xffff0000, v123
	v_pk_mul_f32 v[48:49], v[48:49], s[50:51] op_sel_hi:[1,0]
	v_mul_f32_e32 v11, 0xbfb8aa3b, v27
	v_pk_mul_f32 v[24:25], v[48:49], v[24:25]
	v_lshlrev_b32_e32 v48, 16, v131
	v_exp_f32_e32 v29, v11
	v_mul_f32_e32 v11, v26, v48
	v_and_b32_e32 v49, 0xffff0000, v131
	v_bfe_u32 v15, v11, 16, 1
	v_add3_u32 v11, v11, v15, s51
	ds_write_b16_d16_hi v101, v11 offset:864
	v_sub_f32_e32 v11, v31, v27
	v_mul_f32_e32 v11, 0x3fb8aa3b, v11
	v_exp_f32_e32 v11, v11
	v_pk_mul_f32 v[28:29], v[28:29], v[48:49]
	v_pk_mul_f32 v[50:51], v[50:51], v[52:53]
	v_cvt_pk_bf16_f32 v12, v110, v111
	v_mul_f32_e32 v11, v11, v49
	v_bfe_u32 v15, v11, 16, 1
	v_add3_u32 v11, v11, v15, s51
	ds_write_b16_d16_hi v101, v11 offset:1008
	v_cvt_pk_bf16_f32 v11, v24, v25
	v_mul_f32_e32 v24, 0x3fb8aa3b, v16
	v_mul_f32_e32 v25, 0xbfb8aa3b, v16
	s_waitcnt lgkmcnt(8)
	v_sub_f32_e32 v16, v20, v16
	v_mul_f32_e32 v20, 0x3fb8aa3b, v17
	v_exp_f32_e32 v24, v24
	v_exp_f32_e32 v26, v25
	v_mul_f32_e32 v16, 0x3fb8aa3b, v16
	v_exp_f32_e32 v25, v20
	v_exp_f32_e32 v16, v16
	v_cvt_pk_bf16_f32 v15, v28, v29
	v_lshlrev_b32_e32 v28, 16, v124
	v_and_b32_e32 v29, 0xffff0000, v124
	v_pk_mul_f32 v[28:29], v[28:29], s[50:51] op_sel_hi:[1,0]
	v_mul_f32_e32 v0, 0xbfb8aa3b, v17
	v_pk_mul_f32 v[24:25], v[28:29], v[24:25]
	s_waitcnt vmcnt(0)
	v_lshlrev_b32_e32 v28, 16, v132
	v_exp_f32_e32 v27, v0
	v_mul_f32_e32 v0, v16, v28
	v_and_b32_e32 v29, 0xffff0000, v132
	v_bfe_u32 v4, v0, 16, 1
	v_add3_u32 v0, v0, v4, s51
	ds_write_b16_d16_hi v101, v0 offset:1152
	v_sub_f32_e32 v0, v21, v17
	v_mul_f32_e32 v0, 0x3fb8aa3b, v0
	v_exp_f32_e32 v0, v0
	v_mul_f32_e32 v17, 0xbfb8aa3b, v18
	v_exp_f32_e32 v20, v17
	v_sub_f32_e32 v17, v22, v18
	v_mul_f32_e32 v17, 0x3fb8aa3b, v17
	v_mul_f32_e32 v0, v0, v29
	v_mul_f32_e32 v16, 0x3fb8aa3b, v18
	v_exp_f32_e32 v18, v17
	v_mul_f32_e32 v17, 0x3fb8aa3b, v19
	v_bfe_u32 v4, v0, 16, 1
	v_exp_f32_e32 v16, v16
	v_exp_f32_e32 v17, v17
	v_add3_u32 v0, v0, v4, s51
	ds_write_b16_d16_hi v101, v0 offset:1296
	v_cvt_pk_bf16_f32 v0, v24, v25
	v_lshlrev_b32_e32 v24, 16, v125
	v_and_b32_e32 v25, 0xffff0000, v125
	v_pk_mul_f32 v[24:25], v[24:25], s[50:51] op_sel_hi:[1,0]
	v_mul_f32_e32 v1, 0xbfb8aa3b, v19
	v_pk_mul_f32 v[16:17], v[24:25], v[16:17]
	v_lshlrev_b32_e32 v24, 16, v133
	v_exp_f32_e32 v21, v1
	v_mul_f32_e32 v1, v18, v24
	v_and_b32_e32 v25, 0xffff0000, v133
	v_bfe_u32 v5, v1, 16, 1
	v_add3_u32 v1, v1, v5, s51
	ds_write_b16_d16_hi v101, v1 offset:1440
	v_sub_f32_e32 v1, v23, v19
	v_mul_f32_e32 v1, 0x3fb8aa3b, v1
	v_exp_f32_e32 v1, v1
	v_pk_mul_f32 v[20:21], v[20:21], v[24:25]
	v_pk_mul_f32 v[26:27], v[26:27], v[28:29]
	v_lshlrev_b32_e32 v28, 16, v126
	v_mul_f32_e32 v1, v1, v25
	v_bfe_u32 v5, v1, 16, 1
	v_add3_u32 v1, v1, v5, s51
	ds_write_b16_d16_hi v101, v1 offset:1584
	v_cvt_pk_bf16_f32 v1, v16, v17
	v_cvt_pk_bf16_f32 v5, v20, v21
	ds_read_b128 v[16:19], v98 offset:48
	ds_read_b128 v[20:23], v106 offset:48
	v_cvt_pk_bf16_f32 v4, v26, v27
	v_and_b32_e32 v29, 0xffff0000, v126
	v_pk_mul_f32 v[28:29], v[28:29], s[50:51] op_sel_hi:[1,0]
	s_waitcnt lgkmcnt(1)
	v_mul_f32_e32 v24, 0x3fb8aa3b, v16
	v_mul_f32_e32 v25, 0xbfb8aa3b, v16
	s_waitcnt lgkmcnt(0)
	v_sub_f32_e32 v16, v20, v16
	v_mul_f32_e32 v20, 0x3fb8aa3b, v17
	v_exp_f32_e32 v24, v24
	v_exp_f32_e32 v26, v25
	v_mul_f32_e32 v16, 0x3fb8aa3b, v16
	v_exp_f32_e32 v25, v20
	v_exp_f32_e32 v16, v16
	v_mul_f32_e32 v2, 0xbfb8aa3b, v17
	v_exp_f32_e32 v27, v2
	v_pk_mul_f32 v[24:25], v[28:29], v[24:25]
	v_lshlrev_b32_e32 v28, 16, v134
	v_mul_f32_e32 v2, v16, v28
	v_and_b32_e32 v29, 0xffff0000, v134
	v_bfe_u32 v6, v2, 16, 1
	v_add3_u32 v2, v2, v6, s51
	ds_write_b16_d16_hi v101, v2 offset:1728
	v_sub_f32_e32 v2, v21, v17
	v_mul_f32_e32 v2, 0x3fb8aa3b, v2
	v_exp_f32_e32 v2, v2
	v_mul_f32_e32 v17, 0xbfb8aa3b, v18
	v_exp_f32_e32 v20, v17
	v_sub_f32_e32 v17, v22, v18
	v_mul_f32_e32 v17, 0x3fb8aa3b, v17
	v_mul_f32_e32 v2, v2, v29
	v_mul_f32_e32 v16, 0x3fb8aa3b, v18
	v_exp_f32_e32 v18, v17
	v_mul_f32_e32 v17, 0x3fb8aa3b, v19
	v_bfe_u32 v6, v2, 16, 1
	v_exp_f32_e32 v16, v16
	v_exp_f32_e32 v17, v17
	v_add3_u32 v2, v2, v6, s51
	ds_write_b16_d16_hi v101, v2 offset:1872
	v_cvt_pk_bf16_f32 v2, v24, v25
	v_lshlrev_b32_e32 v24, 16, v127
	v_and_b32_e32 v25, 0xffff0000, v127
	v_pk_mul_f32 v[24:25], v[24:25], s[50:51] op_sel_hi:[1,0]
	v_mul_f32_e32 v3, 0xbfb8aa3b, v19
	v_pk_mul_f32 v[16:17], v[24:25], v[16:17]
	v_lshlrev_b32_e32 v24, 16, v135
	v_exp_f32_e32 v21, v3
	v_mul_f32_e32 v3, v18, v24
	v_and_b32_e32 v25, 0xffff0000, v135
	v_bfe_u32 v7, v3, 16, 1
	v_add3_u32 v3, v3, v7, s51
	ds_write_b16_d16_hi v101, v3 offset:2016
	v_sub_f32_e32 v3, v23, v19
	v_mul_f32_e32 v3, 0x3fb8aa3b, v3
	v_exp_f32_e32 v3, v3
	v_pk_mul_f32 v[26:27], v[26:27], v[28:29]
	v_pk_mul_f32 v[20:21], v[20:21], v[24:25]
	v_cvt_pk_bf16_f32 v14, v50, v51
	v_mul_f32_e32 v3, v3, v25
	v_bfe_u32 v7, v3, 16, 1
	v_add3_u32 v3, v3, v7, s51
	v_cvt_pk_bf16_f32 v6, v26, v27
	ds_write_b16_d16_hi v101, v3 offset:2160
	v_cvt_pk_bf16_f32 v3, v16, v17
	v_cvt_pk_bf16_f32 v7, v20, v21
	ds_write_b128 v102, v[8:11] offset:32768
	ds_write_b128 v102, v[0:3] offset:32784
	ds_write_b128 v102, v[12:15] offset:50176
	ds_write_b128 v102, v[4:7] offset:50192
	v_lshl_add_u64 v[4:5], s[82:83], 0, v[66:67]
	v_lshlrev_b64 v[4:5], 10, v[4:5]
	v_lshl_add_u64 v[4:5], s[80:81], 0, v[4:5]
	v_lshl_add_u64 v[4:5], v[4:5], 0, s[76:77]
	v_lshl_add_u64 v[4:5], v[4:5], 0, v[96:97]
	global_store_dwordx4 v[4:5], v[8:11], off
	global_store_dwordx4 v[4:5], v[0:3], off offset:16
	s_and_saveexec_b64 s[84:85], s[6:7]
	s_cbranch_execz .LBB0_813
	v_add_u32_e32 v0, s86, v90
	ds_read_b32 v0, v0
	s_lshl_b64 s[86:87], s[92:93], 9
	s_waitcnt lgkmcnt(0)
	v_mul_f32_e32 v0, 0x3fb8aa3b, v0
	v_exp_f32_e32 v2, v0
	v_lshl_add_u64 v[0:1], v[68:69], 0, s[86:87]
	global_store_dword v[0:1], v2, off
	s_branch .LBB0_813

.LBB0_915:
	s_and_b32 s92, s87, 3
	s_ashr_i32 s43, s43, 7
	s_add_i32 s84, s43, s76
	s_mul_i32 s43, s86, 0x900
	s_lshl_b32 s91, s92, 8
	s_add_i32 s43, s43, s91
	s_add_i32 s76, s43, 0x400
	s_ashr_i32 s43, s42, 31
	v_lshl_add_u64 v[0:1], v[58:59], 0, s[76:77]
	v_lshl_add_u64 v[2:3], s[42:43], 1, v[60:61]
	v_mad_u64_u32 v[2:3], s[42:43], v0, s75, v[2:3]
	v_mov_b32_e32 v0, v3
	v_mad_u64_u32 v[0:1], s[42:43], v1, s75, v[0:1]
	v_mov_b32_e32 v3, v0
	s_mov_b32 s42, 0x12000
	s_barrier
	global_load_dwordx4 v[44:47], v[2:3], off
	global_load_dwordx4 v[40:43], v[2:3], off offset:64
	v_add_co_u32_e32 v2, vcc, s42, v2
	s_mul_hi_i32 s42, s84, 0x2400
	s_mulk_i32 s84, 0x2400
	s_add_u32 s84, s84, s79
	s_addc_u32 s85, s42, 0
	v_addc_co_u32_e32 v3, vcc, 0, v0, vcc
	v_lshl_add_u64 v[0:1], s[84:85], 0, v[62:63]
	s_lshl_b32 s76, s92, 9
	global_load_dwordx4 v[36:39], v[2:3], off
	global_load_dwordx4 v[32:35], v[2:3], off offset:64
	v_lshl_add_u64 v[2:3], v[64:65], 0, s[76:77]
	v_lshlrev_b64 v[0:1], 11, v[0:1]
	v_lshl_add_u64 v[0:1], v[2:3], 0, v[0:1]
	v_add_co_u32_e32 v2, vcc, s57, v0
	s_add_i32 s76, s78, 0x23f
	s_nop 0
	v_addc_co_u32_e32 v3, vcc, 0, v1, vcc
	v_add_co_u32_e32 v4, vcc, s53, v0
	s_cmpk_lt_u32 s76, 0x47f
	s_nop 0
	v_addc_co_u32_e32 v5, vcc, 0, v1, vcc
	v_add_co_u32_e32 v6, vcc, s70, v0
	s_cselect_b64 s[42:43], -1, 0
	s_nop 0
	v_addc_co_u32_e32 v7, vcc, 0, v1, vcc
	v_add_co_u32_e32 v8, vcc, s62, v0
	s_cmpk_gt_u32 s76, 0x47e
	s_nop 0
	v_addc_co_u32_e32 v9, vcc, 0, v1, vcc
	v_add_co_u32_e32 v10, vcc, s61, v0
	s_cselect_b64 s[86:87], -1, 0
	s_nop 0
	v_addc_co_u32_e32 v11, vcc, 0, v1, vcc
	v_add_co_u32_e32 v12, vcc, s63, v0
	s_mov_b64 s[88:89], -1
	s_nop 0
	v_addc_co_u32_e32 v13, vcc, 0, v1, vcc
	global_load_dword v18, v[4:5], off offset:-4096
	global_load_dword v20, v[4:5], off
	global_load_dword v21, v[4:5], off offset:2048
	global_load_dword v22, v[8:9], off offset:-4096
	global_load_dword v24, v[8:9], off
	global_load_dword v25, v[8:9], off offset:2048
	global_load_dword v26, v[12:13], off offset:-4096
	global_load_dword v28, v[12:13], off
	global_load_dword v29, v[12:13], off offset:2048
	v_add_co_u32_e32 v4, vcc, 0x7000, v0
	s_nop 1
	v_addc_co_u32_e32 v5, vcc, 0, v1, vcc
	global_load_dword v16, v[0:1], off
	global_load_dword v17, v[0:1], off offset:2048
	global_load_dword v19, v[2:3], off offset:2048
	global_load_dword v23, v[6:7], off offset:2048
	global_load_dword v27, v[10:11], off offset:2048
	global_load_dword v30, v[4:5], off
	global_load_dword v31, v[4:5], off offset:2048
	v_add_u32_e32 v114, s79, v66
	v_mov_b64_e32 v[116:117], s[80:81]
	v_mad_i64_i32 v[116:117], vcc, v114, s59, v[116:117]
	s_lshl_b32 s76, s92, 8
	v_lshl_add_u64 v[116:117], v[116:117], 0, s[76:77]
	v_lshl_add_u64 v[116:117], v[116:117], 0, v[96:97]
	s_movk_i32 s76, 0x1800
	v_lshl_add_u64 v[116:117], v[116:117], 0, s[76:77]
	global_load_dwordx4 v[120:123], v[116:117], off
	global_load_dwordx4 v[124:127], v[116:117], off offset:16
	global_load_dwordx4 v[128:131], v[116:117], off offset:1024
	global_load_dwordx4 v[132:135], v[116:117], off offset:1040
	s_and_b64 vcc, exec, s[42:43]
	s_cbranch_vccnz .LBB0_917
	s_waitcnt vmcnt(0)
	v_add_f32_e32 v49, v30, v31
	v_add_f32_e32 v50, v29, v49
	v_add_f32_e32 v51, v28, v50
	v_add_f32_e32 v52, v27, v51
	v_add_f32_e32 v53, v26, v52
	v_add_f32_e32 v54, v25, v53
	v_add_f32_e32 v55, v24, v54
	v_add_f32_e32 v106, v23, v55
	v_add_f32_e32 v107, v22, v106
	v_add_f32_e32 v108, v21, v107
	v_add_f32_e32 v109, v20, v108
	v_add_f32_e32 v110, v19, v109
	v_add_f32_e32 v111, v18, v110
	v_add_f32_e32 v112, v17, v111
	v_mov_b64_e32 v[0:1], v[16:17]
	v_add_f32_e32 v48, v16, v112
	v_mov_b64_e32 v[2:3], v[18:19]
	v_mov_b64_e32 v[4:5], v[20:21]
	v_mov_b64_e32 v[6:7], v[22:23]
	v_mov_b64_e32 v[8:9], v[24:25]
	v_mov_b64_e32 v[10:11], v[26:27]
	v_mov_b64_e32 v[12:13], v[28:29]
	v_mov_b64_e32 v[14:15], v[30:31]
	v_mov_b32_e32 v0, v48
	v_mov_b32_e32 v1, v112
	v_mov_b32_e32 v2, v111
	v_mov_b32_e32 v3, v110
	v_mov_b32_e32 v4, v109
	v_mov_b32_e32 v5, v108
	v_mov_b32_e32 v6, v107
	v_mov_b32_e32 v7, v106
	v_mov_b32_e32 v8, v55
	v_mov_b32_e32 v9, v54
	v_mov_b32_e32 v10, v53
	v_mov_b32_e32 v11, v52
	v_mov_b32_e32 v12, v51
	v_mov_b32_e32 v13, v50
	v_mov_b32_e32 v14, v49
	s_mov_b64 s[88:89], 0

.LBB0_931:
	s_waitcnt vmcnt(6)
	v_add_f32_e32 v0, v0, v16
	v_add_f32_e32 v1, v1, v16
	ds_write2st64_b32 v93, v0, v1 offset1:2
	v_add_f32_e32 v0, v2, v16
	v_add_f32_e32 v1, v3, v16
	ds_write2st64_b32 v93, v0, v1 offset0:4 offset1:6
	v_add_f32_e32 v0, v4, v16
	v_add_f32_e32 v1, v5, v16
	ds_write2st64_b32 v93, v0, v1 offset0:8 offset1:10
	v_add_f32_e32 v0, v6, v16
	v_add_f32_e32 v1, v7, v16
	ds_write2st64_b32 v93, v0, v1 offset0:12 offset1:14
	v_add_f32_e32 v0, v8, v16
	v_add_f32_e32 v1, v9, v16
	ds_write2st64_b32 v93, v0, v1 offset0:16 offset1:18
	v_add_f32_e32 v0, v10, v16
	v_add_f32_e32 v1, v11, v16
	ds_write2st64_b32 v93, v0, v1 offset0:20 offset1:22
	v_add_f32_e32 v0, v12, v16
	v_add_f32_e32 v1, v13, v16
	ds_write2st64_b32 v93, v0, v1 offset0:24 offset1:26
	v_add_f32_e32 v0, v14, v16
	v_add_f32_e32 v1, v15, v16
	ds_write2st64_b32 v93, v0, v1 offset0:28 offset1:30
	v_add_u32_e32 v2, s79, v66
	v_mov_b64_e32 v[0:1], s[80:81]
	v_mad_i64_i32 v[0:1], s[86:87], v2, s59, v[0:1]
	s_lshl_b32 s76, s76, 1
	v_lshl_add_u64 v[0:1], v[0:1], 0, s[76:77]
	v_lshl_add_u64 v[4:5], v[0:1], 0, v[96:97]
	s_mov_b64 s[86:87], 0x1800
	v_add_co_u32_e32 v6, vcc, s57, v4
	v_lshl_add_u64 v[0:1], v[4:5], 0, s[86:87]
	s_nop 0
	v_addc_co_u32_e32 v7, vcc, 0, v5, vcc
	s_waitcnt lgkmcnt(0)
	s_barrier
	s_nop 0
	s_mov_b64 s[86:87], 0x1c00
	v_lshl_add_u64 v[4:5], v[4:5], 0, s[86:87]
	s_nop 0
	ds_read_b128 v[48:51], v98
	s_waitcnt vmcnt(6)
	ds_read_b128 v[24:27], v98 offset:16
	ds_read_b128 v[16:19], v98 offset:32
	v_add_u32_e32 v106, s88, v95
	ds_read_b128 v[52:55], v106
	s_waitcnt vmcnt(4)
	ds_read_b128 v[28:31], v106 offset:16
	ds_read_b128 v[20:23], v106 offset:32
	s_waitcnt lgkmcnt(5)
	v_mul_f32_e32 v107, 0x3fb8aa3b, v48
	v_exp_f32_e32 v108, v107
	v_mul_f32_e32 v107, 0xbfb8aa3b, v48
	s_waitcnt lgkmcnt(2)
	v_sub_f32_e32 v48, v52, v48
	v_mul_f32_e32 v52, 0x3fb8aa3b, v49
	v_mul_f32_e32 v48, 0x3fb8aa3b, v48
	v_exp_f32_e32 v109, v52
	v_exp_f32_e32 v48, v48
	v_exp_f32_e32 v110, v107
	s_ashr_i32 s79, s78, 31
	s_waitcnt vmcnt(3)
	v_lshlrev_b32_e32 v112, 16, v120
	v_and_b32_e32 v113, 0xffff0000, v120
	v_pk_mul_f32 v[112:113], v[112:113], s[50:51] op_sel_hi:[1,0]
	v_mul_f32_e32 v8, 0xbfb8aa3b, v49
	v_pk_mul_f32 v[108:109], v[112:113], v[108:109]
	s_waitcnt vmcnt(1)
	v_lshlrev_b32_e32 v112, 16, v128
	v_exp_f32_e32 v111, v8
	v_mul_f32_e32 v8, v48, v112
	v_and_b32_e32 v113, 0xffff0000, v128
	v_bfe_u32 v12, v8, 16, 1
	v_add3_u32 v8, v8, v12, s51
	ds_write_b16_d16_hi v101, v8
	v_sub_f32_e32 v8, v53, v49
	v_mul_f32_e32 v8, 0x3fb8aa3b, v8
	v_exp_f32_e32 v8, v8
	v_mul_f32_e32 v49, 0xbfb8aa3b, v50
	v_exp_f32_e32 v52, v49
	v_sub_f32_e32 v49, v54, v50
	v_mul_f32_e32 v49, 0x3fb8aa3b, v49
	v_mul_f32_e32 v8, v8, v113
	v_mul_f32_e32 v48, 0x3fb8aa3b, v50
	v_exp_f32_e32 v50, v49
	v_mul_f32_e32 v49, 0x3fb8aa3b, v51
	v_bfe_u32 v12, v8, 16, 1
	v_exp_f32_e32 v48, v48
	v_exp_f32_e32 v49, v49
	v_add3_u32 v8, v8, v12, s51
	ds_write_b16_d16_hi v101, v8 offset:144
	v_cvt_pk_bf16_f32 v8, v108, v109
	v_lshlrev_b32_e32 v108, 16, v121
	v_and_b32_e32 v109, 0xffff0000, v121
	v_pk_mul_f32 v[108:109], v[108:109], s[50:51] op_sel_hi:[1,0]
	v_mul_f32_e32 v9, 0xbfb8aa3b, v51
	v_pk_mul_f32 v[48:49], v[108:109], v[48:49]
	v_lshlrev_b32_e32 v108, 16, v129
	v_exp_f32_e32 v53, v9
	v_mul_f32_e32 v9, v50, v108
	v_and_b32_e32 v109, 0xffff0000, v129
	v_bfe_u32 v13, v9, 16, 1
	v_add3_u32 v9, v9, v13, s51
	ds_write_b16_d16_hi v101, v9 offset:288
	v_sub_f32_e32 v9, v55, v51
	v_mul_f32_e32 v9, 0x3fb8aa3b, v9
	v_exp_f32_e32 v9, v9
	v_pk_mul_f32 v[52:53], v[52:53], v[108:109]
	v_pk_mul_f32 v[110:111], v[110:111], v[112:113]
	v_mul_f32_e32 v9, v9, v109
	v_bfe_u32 v13, v9, 16, 1
	v_add3_u32 v9, v9, v13, s51
	ds_write_b16_d16_hi v101, v9 offset:432
	v_cvt_pk_bf16_f32 v9, v48, v49
	v_mul_f32_e32 v48, 0x3fb8aa3b, v24
	v_mul_f32_e32 v49, 0xbfb8aa3b, v24
	s_waitcnt lgkmcnt(5)
	v_sub_f32_e32 v24, v28, v24
	v_mul_f32_e32 v28, 0x3fb8aa3b, v25
	v_exp_f32_e32 v48, v48
	v_exp_f32_e32 v50, v49
	v_mul_f32_e32 v24, 0x3fb8aa3b, v24
	v_exp_f32_e32 v49, v28
	v_exp_f32_e32 v24, v24
	v_cvt_pk_bf16_f32 v13, v52, v53
	v_lshlrev_b32_e32 v52, 16, v122
	v_and_b32_e32 v53, 0xffff0000, v122
	v_pk_mul_f32 v[52:53], v[52:53], s[50:51] op_sel_hi:[1,0]
	v_mul_f32_e32 v10, 0xbfb8aa3b, v25
	v_pk_mul_f32 v[48:49], v[52:53], v[48:49]
	v_lshlrev_b32_e32 v52, 16, v130
	v_exp_f32_e32 v51, v10
	v_mul_f32_e32 v10, v24, v52
	v_and_b32_e32 v53, 0xffff0000, v130
	v_bfe_u32 v14, v10, 16, 1
	v_add3_u32 v10, v10, v14, s51
	ds_write_b16_d16_hi v101, v10 offset:576
	v_sub_f32_e32 v10, v29, v25
	v_mul_f32_e32 v10, 0x3fb8aa3b, v10
	v_exp_f32_e32 v10, v10
	v_mul_f32_e32 v25, 0xbfb8aa3b, v26
	v_exp_f32_e32 v28, v25
	v_sub_f32_e32 v25, v30, v26
	v_mul_f32_e32 v25, 0x3fb8aa3b, v25
	v_mul_f32_e32 v10, v10, v53
	v_mul_f32_e32 v24, 0x3fb8aa3b, v26
	v_exp_f32_e32 v26, v25
	v_mul_f32_e32 v25, 0x3fb8aa3b, v27
	v_bfe_u32 v14, v10, 16, 1
	v_exp_f32_e32 v24, v24
	v_exp_f32_e32 v25, v25
	v_add3_u32 v10, v10, v14, s51
	ds_write_b16_d16_hi v101, v10 offset:720
	v_cvt_pk_bf16_f32 v10, v48, v49
	v_lshlrev_b32_e32 v48, 16, v123
	v_and_b32_e32 v49, 0xffff0000, v123
	v_pk_mul_f32 v[48:49], v[48:49], s[50:51] op_sel_hi:[1,0]
	v_mul_f32_e32 v11, 0xbfb8aa3b, v27
	v_pk_mul_f32 v[24:25], v[48:49], v[24:25]
	v_lshlrev_b32_e32 v48, 16, v131
	v_exp_f32_e32 v29, v11
	v_mul_f32_e32 v11, v26, v48
	v_and_b32_e32 v49, 0xffff0000, v131
	v_bfe_u32 v15, v11, 16, 1
	v_add3_u32 v11, v11, v15, s51
	ds_write_b16_d16_hi v101, v11 offset:864
	v_sub_f32_e32 v11, v31, v27
	v_mul_f32_e32 v11, 0x3fb8aa3b, v11
	v_exp_f32_e32 v11, v11
	v_pk_mul_f32 v[28:29], v[28:29], v[48:49]
	v_pk_mul_f32 v[50:51], v[50:51], v[52:53]
	v_cvt_pk_bf16_f32 v12, v110, v111
	v_mul_f32_e32 v11, v11, v49
	v_bfe_u32 v15, v11, 16, 1
	v_add3_u32 v11, v11, v15, s51
	ds_write_b16_d16_hi v101, v11 offset:1008
	v_cvt_pk_bf16_f32 v11, v24, v25
	v_mul_f32_e32 v24, 0x3fb8aa3b, v16
	v_mul_f32_e32 v25, 0xbfb8aa3b, v16
	s_waitcnt lgkmcnt(8)
	v_sub_f32_e32 v16, v20, v16
	v_mul_f32_e32 v20, 0x3fb8aa3b, v17
	v_exp_f32_e32 v24, v24
	v_exp_f32_e32 v26, v25
	v_mul_f32_e32 v16, 0x3fb8aa3b, v16
	v_exp_f32_e32 v25, v20
	v_exp_f32_e32 v16, v16
	v_cvt_pk_bf16_f32 v15, v28, v29
	v_lshlrev_b32_e32 v28, 16, v124
	v_and_b32_e32 v29, 0xffff0000, v124
	v_pk_mul_f32 v[28:29], v[28:29], s[50:51] op_sel_hi:[1,0]
	v_mul_f32_e32 v0, 0xbfb8aa3b, v17
	v_pk_mul_f32 v[24:25], v[28:29], v[24:25]
	s_waitcnt vmcnt(0)
	v_lshlrev_b32_e32 v28, 16, v132
	v_exp_f32_e32 v27, v0
	v_mul_f32_e32 v0, v16, v28
	v_and_b32_e32 v29, 0xffff0000, v132
	v_bfe_u32 v4, v0, 16, 1
	v_add3_u32 v0, v0, v4, s51
	ds_write_b16_d16_hi v101, v0 offset:1152
	v_sub_f32_e32 v0, v21, v17
	v_mul_f32_e32 v0, 0x3fb8aa3b, v0
	v_exp_f32_e32 v0, v0
	v_mul_f32_e32 v17, 0xbfb8aa3b, v18
	v_exp_f32_e32 v20, v17
	v_sub_f32_e32 v17, v22, v18
	v_mul_f32_e32 v17, 0x3fb8aa3b, v17
	v_mul_f32_e32 v0, v0, v29
	v_mul_f32_e32 v16, 0x3fb8aa3b, v18
	v_exp_f32_e32 v18, v17
	v_mul_f32_e32 v17, 0x3fb8aa3b, v19
	v_bfe_u32 v4, v0, 16, 1
	v_exp_f32_e32 v16, v16
	v_exp_f32_e32 v17, v17
	v_add3_u32 v0, v0, v4, s51
	ds_write_b16_d16_hi v101, v0 offset:1296
	v_cvt_pk_bf16_f32 v0, v24, v25
	v_lshlrev_b32_e32 v24, 16, v125
	v_and_b32_e32 v25, 0xffff0000, v125
	v_pk_mul_f32 v[24:25], v[24:25], s[50:51] op_sel_hi:[1,0]
	v_mul_f32_e32 v1, 0xbfb8aa3b, v19
	v_pk_mul_f32 v[16:17], v[24:25], v[16:17]
	v_lshlrev_b32_e32 v24, 16, v133
	v_exp_f32_e32 v21, v1
	v_mul_f32_e32 v1, v18, v24
	v_and_b32_e32 v25, 0xffff0000, v133
	v_bfe_u32 v5, v1, 16, 1
	v_add3_u32 v1, v1, v5, s51
	ds_write_b16_d16_hi v101, v1 offset:1440
	v_sub_f32_e32 v1, v23, v19
	v_mul_f32_e32 v1, 0x3fb8aa3b, v1
	v_exp_f32_e32 v1, v1
	v_pk_mul_f32 v[20:21], v[20:21], v[24:25]
	v_pk_mul_f32 v[26:27], v[26:27], v[28:29]
	v_lshlrev_b32_e32 v28, 16, v126
	v_mul_f32_e32 v1, v1, v25
	v_bfe_u32 v5, v1, 16, 1
	v_add3_u32 v1, v1, v5, s51
	ds_write_b16_d16_hi v101, v1 offset:1584
	v_cvt_pk_bf16_f32 v1, v16, v17
	v_cvt_pk_bf16_f32 v5, v20, v21
	ds_read_b128 v[16:19], v98 offset:48
	ds_read_b128 v[20:23], v106 offset:48
	v_cvt_pk_bf16_f32 v4, v26, v27
	v_and_b32_e32 v29, 0xffff0000, v126
	v_pk_mul_f32 v[28:29], v[28:29], s[50:51] op_sel_hi:[1,0]
	s_waitcnt lgkmcnt(1)
	v_mul_f32_e32 v24, 0x3fb8aa3b, v16
	v_mul_f32_e32 v25, 0xbfb8aa3b, v16
	s_waitcnt lgkmcnt(0)
	v_sub_f32_e32 v16, v20, v16
	v_mul_f32_e32 v20, 0x3fb8aa3b, v17
	v_exp_f32_e32 v24, v24
	v_exp_f32_e32 v26, v25
	v_mul_f32_e32 v16, 0x3fb8aa3b, v16
	v_exp_f32_e32 v25, v20
	v_exp_f32_e32 v16, v16
	v_mul_f32_e32 v2, 0xbfb8aa3b, v17
	v_exp_f32_e32 v27, v2
	v_pk_mul_f32 v[24:25], v[28:29], v[24:25]
	v_lshlrev_b32_e32 v28, 16, v134
	v_mul_f32_e32 v2, v16, v28
	v_and_b32_e32 v29, 0xffff0000, v134
	v_bfe_u32 v6, v2, 16, 1
	v_add3_u32 v2, v2, v6, s51
	ds_write_b16_d16_hi v101, v2 offset:1728
	v_sub_f32_e32 v2, v21, v17
	v_mul_f32_e32 v2, 0x3fb8aa3b, v2
	v_exp_f32_e32 v2, v2
	v_mul_f32_e32 v17, 0xbfb8aa3b, v18
	v_exp_f32_e32 v20, v17
	v_sub_f32_e32 v17, v22, v18
	v_mul_f32_e32 v17, 0x3fb8aa3b, v17
	v_mul_f32_e32 v2, v2, v29
	v_mul_f32_e32 v16, 0x3fb8aa3b, v18
	v_exp_f32_e32 v18, v17
	v_mul_f32_e32 v17, 0x3fb8aa3b, v19
	v_bfe_u32 v6, v2, 16, 1
	v_exp_f32_e32 v16, v16
	v_exp_f32_e32 v17, v17
	v_add3_u32 v2, v2, v6, s51
	ds_write_b16_d16_hi v101, v2 offset:1872
	v_cvt_pk_bf16_f32 v2, v24, v25
	v_lshlrev_b32_e32 v24, 16, v127
	v_and_b32_e32 v25, 0xffff0000, v127
	v_pk_mul_f32 v[24:25], v[24:25], s[50:51] op_sel_hi:[1,0]
	v_mul_f32_e32 v3, 0xbfb8aa3b, v19
	v_pk_mul_f32 v[16:17], v[24:25], v[16:17]
	v_lshlrev_b32_e32 v24, 16, v135
	v_exp_f32_e32 v21, v3
	v_mul_f32_e32 v3, v18, v24
	v_and_b32_e32 v25, 0xffff0000, v135
	v_bfe_u32 v7, v3, 16, 1
	v_add3_u32 v3, v3, v7, s51
	ds_write_b16_d16_hi v101, v3 offset:2016
	v_sub_f32_e32 v3, v23, v19
	v_mul_f32_e32 v3, 0x3fb8aa3b, v3
	v_exp_f32_e32 v3, v3
	v_pk_mul_f32 v[26:27], v[26:27], v[28:29]
	v_pk_mul_f32 v[20:21], v[20:21], v[24:25]
	v_cvt_pk_bf16_f32 v14, v50, v51
	v_mul_f32_e32 v3, v3, v25
	v_bfe_u32 v7, v3, 16, 1
	v_add3_u32 v3, v3, v7, s51
	v_cvt_pk_bf16_f32 v6, v26, v27
	ds_write_b16_d16_hi v101, v3 offset:2160
	v_cvt_pk_bf16_f32 v3, v16, v17
	v_cvt_pk_bf16_f32 v7, v20, v21
	ds_write_b128 v102, v[8:11] offset:32768
	ds_write_b128 v102, v[0:3] offset:32784
	ds_write_b128 v102, v[12:15] offset:50176
	ds_write_b128 v102, v[4:7] offset:50192
	v_lshl_add_u64 v[4:5], s[84:85], 0, v[66:67]
	v_lshlrev_b64 v[4:5], 10, v[4:5]
	v_lshl_add_u64 v[4:5], s[82:83], 0, v[4:5]
	v_lshl_add_u64 v[4:5], v[4:5], 0, s[76:77]
	v_lshl_add_u64 v[4:5], v[4:5], 0, v[96:97]
	global_store_dwordx4 v[4:5], v[8:11], off
	global_store_dwordx4 v[4:5], v[0:3], off offset:16
	s_and_saveexec_b64 s[86:87], s[6:7]
	s_cbranch_execz .LBB0_910
	v_add_u32_e32 v0, s88, v90
	ds_read_b32 v0, v0
	s_lshl_b64 s[88:89], s[78:79], 9
	s_waitcnt lgkmcnt(0)
	v_mul_f32_e32 v0, 0x3fb8aa3b, v0
	v_exp_f32_e32 v2, v0
	v_lshl_add_u64 v[0:1], v[68:69], 0, s[88:89]
	global_store_dword v[0:1], v2, off
	s_branch .LBB0_910

.LBB0_1050:
	s_andn2_b64 vcc, exec, s[2:3]
	s_cbranch_vccnz .LBB0_1116
	v_readlane_b32 s2, v255, 35
	v_readlane_b32 s3, v255, 36
	s_and_b64 s[2:3], s[2:3], exec
	s_cselect_b32 s13, 4, 0
	s_xor_b32 s14, s13, 36
	s_lshl_b32 s15, s14, 4
	s_cmp_ge_i32 s12, s15
	s_cbranch_scc1 .LBB0_1062
	s_ashr_i32 s9, s8, 6
	s_add_u32 s4, s44, 0x1d518000
	s_addc_u32 s5, s45, 0
	s_add_u32 s6, s44, 0x22f18000
	v_readlane_b32 s2, v255, 37
	s_addc_u32 s7, s45, 0
	v_readlane_b32 s3, v255, 38
	s_lshl_b32 s76, s2, 8
	v_readlane_b32 s16, v254, 55
	s_lshl_b64 s[2:3], s[76:77], 2
	v_readlane_b32 s28, v255, 3
	v_readlane_b32 s29, v255, 4
	s_add_u32 s10, s28, s2
	s_addc_u32 s11, s29, s3
	s_lshl_b32 s2, s9, 5
	s_and_b32 s16, s9, 3
	s_and_b32 s9, s2, 0xffffff80
	v_lshrrev_b32_e32 v1, 2, v0
	v_and_b32_e32 v96, 48, v0
	v_and_b32_e32 v4, 63, v0
	v_and_b32_e32 v2, 15, v0
	v_and_or_b32 v44, v1, 12, s9
	v_lshl_add_u64 v[0:1], s[44:45], 0, v[96:97]
	s_mov_b64 s[2:3], 0x64dc8000
	v_lshl_add_u64 v[46:47], v[0:1], 0, s[2:3]
	s_ashr_i32 s2, s9, 31
	v_lshl_add_u32 v5, v2, 2, 0
	v_lshl_or_b32 v62, s16, 4, v2
	v_lshlrev_b32_e32 v2, 6, v2
	v_mov_b32_e32 v3, s2
	v_ashrrev_i32_e32 v45, 31, v44
	v_lshl_add_u32 v2, s9, 8, v2
	v_add_u32_e32 v65, v2, v96
	v_lshl_add_u64 v[48:49], v[44:45], 2, s[10:11]
	v_lshl_add_u64 v[0:1], v[0:1], 0, v[2:3]
	s_mov_b64 s[10:11], 0x27718000
	v_lshl_add_u64 v[50:51], v[0:1], 0, s[10:11]
	v_lshlrev_b32_e32 v102, 4, v4
	s_lshl_b32 s100, s66, 7
	v_add_u32_e32 v102, s100, v102
	v_mov_b32_e32 v103, v97
	v_lshl_add_u64 v[102:103], s[44:45], 0, v[102:103]
	v_lshl_add_u64 v[102:103], v[102:103], 0, s[10:11]
	v_cvt_f32_ubyte0_e32 v0, s14
	v_rcp_iflag_f32_e32 v0, v0
	s_lshl_b32 s9, s16, 6
	v_add_u32_e32 v63, s9, v5
	v_add_u32_e32 v63, 0x20a00, v63
	s_sub_i32 s9, 0, s14
	v_mul_f32_e32 v0, 0x4f7ffffe, v0
	v_cvt_u32_f32_e32 v0, v0
	v_lshl_add_u32 v6, v4, 2, 0
	s_andn2_b32 s8, s8, 63
	v_cmp_gt_u32_e64 s[2:3], 16, v4
	v_readfirstlane_b32 s10, v0
	s_mul_i32 s9, s9, s10
	s_mul_hi_u32 s9, s10, s9
	s_add_i32 s16, s10, s9
	v_add_u32_e32 v64, s8, v6
	v_add_u32_e32 v64, 0x20a00, v64
	v_readlane_b32 s17, v254, 56
	v_readlane_b32 s18, v254, 57
	v_readlane_b32 s19, v254, 58
	v_readlane_b32 s20, v254, 59
	v_readlane_b32 s21, v254, 60
	v_readlane_b32 s22, v254, 61
	v_readlane_b32 s23, v254, 62
	v_readlane_b32 s24, v254, 63
	v_readlane_b32 s25, v255, 0
	v_readlane_b32 s26, v255, 1
	v_readlane_b32 s27, v255, 2
	v_readlane_b32 s30, v255, 5
	v_readlane_b32 s31, v255, 6
	s_branch .LBB0_1054
.LBB0_1053:
	s_or_b64 exec, exec, s[10:11]
	s_waitcnt lgkmcnt(0)
	s_barrier
	ds_read2st64_b32 v[32:33], v63 offset1:1
	v_mov_b64_e32 v[34:35], s[44:45]
	v_mad_i64_i32 v[34:35], s[10:11], v52, s59, v[34:35]
	s_lshl_b32 s76, s8, 1
	s_waitcnt lgkmcnt(0)
	v_add_f32_e32 v32, v32, v33
	v_mov_b32_e32 v33, 0x358637bd
	v_fmamk_f32 v32, v32, 0x3b800000, v33
	v_cmp_gt_f32_e32 vcc, s33, v32
	v_mul_f32_e32 v33, 0x4b800000, v32
	v_lshl_add_u64 v[34:35], v[34:35], 0, s[76:77]
	v_cndmask_b32_e32 v32, v32, v33, vcc
	v_rsq_f32_e32 v32, v32
	v_lshl_add_u64 v[36:37], s[6:7], 0, v[54:55]
	v_lshlrev_b64 v[42:43], 1, v[44:45]
	v_lshl_add_u64 v[40:41], v[36:37], 0, s[76:77]
	v_lshl_add_u64 v[36:37], v[34:35], 0, v[42:43]
	s_mov_b64 s[8:9], 0xbcfa800
	v_mul_f32_e32 v33, 0x45800000, v32
	v_lshl_add_u64 v[34:35], v[36:37], 0, s[8:9]
	s_mov_b32 s8, 0xbcfa000
	v_cndmask_b32_e32 v32, v32, v33, vcc
	v_add_co_u32_e32 v36, vcc, s8, v36
	s_add_i32 s12, s12, s96
	s_nop 0
	v_addc_co_u32_e32 v37, vcc, 0, v37, vcc
	s_nop 0
	s_cmp_lt_i32 s12, s15
	v_lshlrev_b32_e32 v54, 16, v184
	v_mul_f32_e32 v33, 0xbfb8aa3b, v54
	v_exp_f32_e32 v33, v33
	v_and_b32_e32 v55, 0xffff0000, v184
	v_add_f32_e32 v33, 1.0, v33
	v_rcp_f32_e32 v56, v33
	v_pk_mul_f32 v[28:29], v[28:29], v[32:33] op_sel_hi:[1,0]
	v_mul_f32_e32 v33, 0xbfb8aa3b, v55
	v_exp_f32_e32 v33, v33
	v_pk_mul_f32 v[28:29], v[200:201], v[28:29]
	v_lshlrev_b32_e32 v36, 16, v185
	v_and_b32_e32 v37, 0xffff0000, v185
	v_add_f32_e32 v33, 1.0, v33
	v_rcp_f32_e32 v57, v33
	v_mul_f32_e32 v33, 0xbfb8aa3b, v36
	v_exp_f32_e32 v33, v33
	v_pk_mul_f32 v[28:29], v[28:29], v[54:55]
	v_add_f32_e32 v33, 1.0, v33
	v_rcp_f32_e32 v52, v33
	v_pk_mul_f32 v[30:31], v[30:31], v[32:33] op_sel_hi:[1,0]
	v_mul_f32_e32 v33, 0xbfb8aa3b, v37
	v_exp_f32_e32 v33, v33
	v_pk_mul_f32 v[30:31], v[202:203], v[30:31]
	v_pk_mul_f32 v[28:29], v[56:57], v[28:29]
	v_pk_mul_f32 v[30:31], v[30:31], v[36:37]
	v_add_f32_e32 v33, 1.0, v33
	v_rcp_f32_e32 v53, v33
	v_pk_mul_f32 v[24:25], v[24:25], v[32:33] op_sel_hi:[1,0]
	v_pk_mul_f32 v[36:37], v[52:53], v[30:31]
	v_cvt_pk_bf16_f32 v30, v28, v29
	v_cvt_pk_bf16_f32 v31, v36, v37
	v_lshl_add_u64 v[28:29], v[40:41], 0, v[42:43]
	global_store_dwordx2 v[28:29], v[30:31], off
	s_nop 0
	v_lshlrev_b32_e32 v40, 16, v186
	v_and_b32_e32 v41, 0xffff0000, v186
	v_mul_f32_e32 v30, 0xbfb8aa3b, v40
	v_exp_f32_e32 v30, v30
	v_pk_mul_f32 v[24:25], v[204:205], v[24:25]
	v_add_f32_e32 v30, 1.0, v30
	v_rcp_f32_e32 v42, v30
	v_mul_f32_e32 v30, 0xbfb8aa3b, v41
	v_exp_f32_e32 v30, v30
	v_pk_mul_f32 v[24:25], v[24:25], v[40:41]
	v_add_f32_e32 v30, 1.0, v30
	v_rcp_f32_e32 v43, v30
	v_lshlrev_b32_e32 v30, 16, v187
	v_mul_f32_e32 v33, 0xbfb8aa3b, v30
	v_exp_f32_e32 v33, v33
	v_and_b32_e32 v31, 0xffff0000, v187
	v_pk_mul_f32 v[24:25], v[24:25], v[42:43]
	v_add_f32_e32 v33, 1.0, v33
	v_pk_mul_f32 v[26:27], v[26:27], v[32:33] op_sel_hi:[1,0]
	v_rcp_f32_e32 v36, v33
	v_pk_mul_f32 v[26:27], v[206:207], v[26:27]
	v_cvt_pk_bf16_f32 v24, v24, v25
	v_pk_mul_f32 v[26:27], v[26:27], v[30:31]
	v_mul_f32_e32 v30, 0xbfb8aa3b, v31
	v_exp_f32_e32 v30, v30
	v_pk_mul_f32 v[20:21], v[20:21], v[32:33] op_sel_hi:[1,0]
	v_pk_mul_f32 v[22:23], v[22:23], v[32:33] op_sel_hi:[1,0]
	v_pk_mul_f32 v[12:13], v[12:13], v[32:33] op_sel_hi:[1,0]
	v_add_f32_e32 v30, 1.0, v30
	v_rcp_f32_e32 v37, v30
	v_pk_mul_f32 v[14:15], v[14:15], v[32:33] op_sel_hi:[1,0]
	v_pk_mul_f32 v[16:17], v[16:17], v[32:33] op_sel_hi:[1,0]
	v_pk_mul_f32 v[18:19], v[18:19], v[32:33] op_sel_hi:[1,0]
	v_pk_mul_f32 v[26:27], v[26:27], v[36:37]
	v_pk_mul_f32 v[8:9], v[8:9], v[32:33] op_sel_hi:[1,0]
	v_cvt_pk_bf16_f32 v25, v26, v27
	global_store_dwordx2 v[28:29], v[24:25], off offset:32
	s_nop 0
	v_pk_mul_f32 v[10:11], v[10:11], v[32:33] op_sel_hi:[1,0]
	v_pk_mul_f32 v[4:5], v[4:5], v[32:33] op_sel_hi:[1,0]
	v_pk_mul_f32 v[6:7], v[6:7], v[32:33] op_sel_hi:[1,0]
	v_pk_mul_f32 v[0:1], v[0:1], v[32:33] op_sel_hi:[1,0]
	v_pk_mul_f32 v[2:3], v[2:3], v[32:33] op_sel_hi:[1,0]
	v_and_b32_e32 v37, 0xffff0000, v188
	v_lshlrev_b32_e32 v36, 16, v188
	v_pk_mul_f32 v[20:21], v[20:21], v[208:209]
	v_mul_f32_e32 v24, 0xbfb8aa3b, v37
	v_mul_f32_e32 v30, 0xbfb8aa3b, v36
	v_exp_f32_e32 v24, v24
	v_exp_f32_e32 v30, v30
	v_and_b32_e32 v25, 0xffff0000, v189
	v_pk_mul_f32 v[22:23], v[22:23], v[210:211]
	v_add_f32_e32 v24, 1.0, v24
	v_add_f32_e32 v30, 1.0, v30
	v_rcp_f32_e32 v39, v24
	v_lshlrev_b32_e32 v24, 16, v189
	v_rcp_f32_e32 v38, v30
	v_mul_f32_e32 v30, 0xbfb8aa3b, v24
	v_pk_mul_f32 v[22:23], v[22:23], v[24:25]
	v_mul_f32_e32 v24, 0xbfb8aa3b, v25
	v_exp_f32_e32 v30, v30
	v_exp_f32_e32 v24, v24
	v_pk_mul_f32 v[20:21], v[20:21], v[36:37]
	v_add_f32_e32 v30, 1.0, v30
	v_add_f32_e32 v24, 1.0, v24
	v_rcp_f32_e32 v30, v30
	v_rcp_f32_e32 v31, v24
	v_pk_mul_f32 v[20:21], v[20:21], v[38:39]
	v_pk_mul_f32 v[22:23], v[22:23], v[30:31]
	v_cvt_pk_bf16_f32 v20, v20, v21
	v_cvt_pk_bf16_f32 v21, v22, v23
	global_store_dwordx2 v[28:29], v[20:21], off offset:64
	s_nop 0
	v_and_b32_e32 v27, 0xffff0000, v190
	v_lshlrev_b32_e32 v26, 16, v190
	v_pk_mul_f32 v[12:13], v[12:13], v[212:213]
	v_mul_f32_e32 v20, 0xbfb8aa3b, v27
	v_mul_f32_e32 v24, 0xbfb8aa3b, v26
	v_exp_f32_e32 v20, v20
	v_exp_f32_e32 v24, v24
	v_and_b32_e32 v21, 0xffff0000, v191
	v_pk_mul_f32 v[14:15], v[14:15], v[214:215]
	v_add_f32_e32 v20, 1.0, v20
	v_add_f32_e32 v24, 1.0, v24
	v_rcp_f32_e32 v31, v20
	v_lshlrev_b32_e32 v20, 16, v191
	v_rcp_f32_e32 v30, v24
	v_mul_f32_e32 v24, 0xbfb8aa3b, v20
	v_pk_mul_f32 v[14:15], v[14:15], v[20:21]
	v_mul_f32_e32 v20, 0xbfb8aa3b, v21
	v_exp_f32_e32 v24, v24
	v_exp_f32_e32 v20, v20
	v_pk_mul_f32 v[12:13], v[12:13], v[26:27]
	v_add_f32_e32 v24, 1.0, v24
	v_add_f32_e32 v20, 1.0, v20
	v_rcp_f32_e32 v24, v24
	v_rcp_f32_e32 v25, v20
	v_pk_mul_f32 v[12:13], v[12:13], v[30:31]
	v_pk_mul_f32 v[14:15], v[14:15], v[24:25]
	v_cvt_pk_bf16_f32 v12, v12, v13
	v_cvt_pk_bf16_f32 v13, v14, v15
	global_store_dwordx2 v[28:29], v[12:13], off offset:96
	s_nop 0
	v_and_b32_e32 v23, 0xffff0000, v192
	v_lshlrev_b32_e32 v22, 16, v192
	v_pk_mul_f32 v[12:13], v[16:17], v[218:219]
	v_mul_f32_e32 v16, 0xbfb8aa3b, v23
	v_mul_f32_e32 v20, 0xbfb8aa3b, v22
	v_exp_f32_e32 v16, v16
	v_exp_f32_e32 v20, v20
	v_and_b32_e32 v17, 0xffff0000, v193
	v_pk_mul_f32 v[14:15], v[18:19], v[220:221]
	v_add_f32_e32 v16, 1.0, v16
	v_add_f32_e32 v20, 1.0, v20
	v_rcp_f32_e32 v25, v16
	v_lshlrev_b32_e32 v16, 16, v193
	v_rcp_f32_e32 v24, v20
	v_mul_f32_e32 v20, 0xbfb8aa3b, v16
	v_pk_mul_f32 v[14:15], v[14:15], v[16:17]
	v_mul_f32_e32 v16, 0xbfb8aa3b, v17
	v_exp_f32_e32 v20, v20
	v_exp_f32_e32 v16, v16
	v_pk_mul_f32 v[12:13], v[12:13], v[22:23]
	v_add_f32_e32 v20, 1.0, v20
	v_add_f32_e32 v16, 1.0, v16
	v_rcp_f32_e32 v20, v20
	v_rcp_f32_e32 v21, v16
	v_pk_mul_f32 v[12:13], v[12:13], v[24:25]
	v_pk_mul_f32 v[14:15], v[14:15], v[20:21]
	v_cvt_pk_bf16_f32 v12, v12, v13
	v_cvt_pk_bf16_f32 v13, v14, v15
	global_store_dwordx2 v[28:29], v[12:13], off offset:128
	s_nop 0
	v_and_b32_e32 v19, 0xffff0000, v194
	v_lshlrev_b32_e32 v18, 16, v194
	v_pk_mul_f32 v[8:9], v[8:9], v[222:223]
	v_mul_f32_e32 v12, 0xbfb8aa3b, v19
	v_mul_f32_e32 v16, 0xbfb8aa3b, v18
	v_exp_f32_e32 v12, v12
	v_exp_f32_e32 v16, v16
	v_and_b32_e32 v13, 0xffff0000, v195
	v_pk_mul_f32 v[10:11], v[10:11], v[224:225]
	v_add_f32_e32 v12, 1.0, v12
	v_add_f32_e32 v16, 1.0, v16
	v_rcp_f32_e32 v21, v12
	v_lshlrev_b32_e32 v12, 16, v195
	v_rcp_f32_e32 v20, v16
	v_mul_f32_e32 v16, 0xbfb8aa3b, v12
	v_pk_mul_f32 v[10:11], v[10:11], v[12:13]
	v_mul_f32_e32 v12, 0xbfb8aa3b, v13
	v_exp_f32_e32 v16, v16
	v_exp_f32_e32 v12, v12
	v_pk_mul_f32 v[8:9], v[8:9], v[18:19]
	v_add_f32_e32 v16, 1.0, v16
	v_add_f32_e32 v12, 1.0, v12
	v_rcp_f32_e32 v16, v16
	v_rcp_f32_e32 v17, v12
	v_pk_mul_f32 v[8:9], v[8:9], v[20:21]
	v_pk_mul_f32 v[10:11], v[10:11], v[16:17]
	v_cvt_pk_bf16_f32 v8, v8, v9
	v_cvt_pk_bf16_f32 v9, v10, v11
	global_store_dwordx2 v[28:29], v[8:9], off offset:160
	s_nop 0
	v_and_b32_e32 v15, 0xffff0000, v196
	v_lshlrev_b32_e32 v14, 16, v196
	v_pk_mul_f32 v[4:5], v[4:5], v[226:227]
	v_mul_f32_e32 v8, 0xbfb8aa3b, v15
	v_mul_f32_e32 v12, 0xbfb8aa3b, v14
	v_exp_f32_e32 v8, v8
	v_exp_f32_e32 v12, v12
	v_and_b32_e32 v9, 0xffff0000, v197
	v_pk_mul_f32 v[6:7], v[6:7], v[228:229]
	v_add_f32_e32 v8, 1.0, v8
	v_add_f32_e32 v12, 1.0, v12
	v_rcp_f32_e32 v17, v8
	v_lshlrev_b32_e32 v8, 16, v197
	v_rcp_f32_e32 v16, v12
	v_mul_f32_e32 v12, 0xbfb8aa3b, v8
	v_pk_mul_f32 v[6:7], v[6:7], v[8:9]
	v_mul_f32_e32 v8, 0xbfb8aa3b, v9
	v_exp_f32_e32 v12, v12
	v_exp_f32_e32 v8, v8
	v_pk_mul_f32 v[4:5], v[4:5], v[14:15]
	v_add_f32_e32 v12, 1.0, v12
	v_add_f32_e32 v8, 1.0, v8
	v_rcp_f32_e32 v12, v12
	v_rcp_f32_e32 v13, v8
	v_pk_mul_f32 v[4:5], v[4:5], v[16:17]
	v_pk_mul_f32 v[6:7], v[6:7], v[12:13]
	v_cvt_pk_bf16_f32 v4, v4, v5
	v_cvt_pk_bf16_f32 v5, v6, v7
	global_store_dwordx2 v[28:29], v[4:5], off offset:192
	s_nop 0
	v_and_b32_e32 v11, 0xffff0000, v198
	v_lshlrev_b32_e32 v10, 16, v198
	v_pk_mul_f32 v[0:1], v[0:1], v[230:231]
	v_mul_f32_e32 v4, 0xbfb8aa3b, v11
	v_mul_f32_e32 v8, 0xbfb8aa3b, v10
	v_exp_f32_e32 v4, v4
	v_exp_f32_e32 v8, v8
	v_and_b32_e32 v5, 0xffff0000, v199
	v_pk_mul_f32 v[2:3], v[2:3], v[232:233]
	v_add_f32_e32 v4, 1.0, v4
	v_add_f32_e32 v8, 1.0, v8
	v_rcp_f32_e32 v13, v4
	v_lshlrev_b32_e32 v4, 16, v199
	v_rcp_f32_e32 v12, v8
	v_mul_f32_e32 v8, 0xbfb8aa3b, v4
	v_pk_mul_f32 v[2:3], v[2:3], v[4:5]
	v_mul_f32_e32 v4, 0xbfb8aa3b, v5
	v_exp_f32_e32 v8, v8
	v_exp_f32_e32 v4, v4
	v_pk_mul_f32 v[0:1], v[0:1], v[10:11]
	v_add_f32_e32 v8, 1.0, v8
	v_add_f32_e32 v4, 1.0, v4
	v_rcp_f32_e32 v8, v8
	v_rcp_f32_e32 v9, v4
	v_pk_mul_f32 v[0:1], v[0:1], v[12:13]
	v_pk_mul_f32 v[2:3], v[2:3], v[8:9]
	v_cvt_pk_bf16_f32 v0, v0, v1
	v_cvt_pk_bf16_f32 v1, v2, v3
	global_store_dwordx2 v[28:29], v[0:1], off offset:224
	s_cbranch_scc0 .LBB0_1062

.LBB0_1058:
	s_and_b32 s9, s12, 3
	v_add_u32_e32 v52, s11, v62
	v_ashrrev_i32_e32 v53, 31, v52
	s_lshl_b32 s8, s9, 8
	v_add_u32_e32 v0, s8, v44
	v_lshlrev_b64 v[54:55], 11, v[52:53]
	v_lshl_add_u64 v[2:3], s[4:5], 0, v[54:55]
	v_ashrrev_i32_e32 v1, 31, v0
	v_lshl_add_u64 v[0:1], v[0:1], 1, v[2:3]
	s_mov_b64 s[18:19], 0x1200000
	v_add_co_u32_e32 v28, vcc, 0x1200000, v0
	v_lshl_add_u64 v[16:17], v[0:1], 0, s[18:19]
	s_nop 0
	v_addc_co_u32_e32 v29, vcc, 0, v1, vcc
	global_load_dwordx2 v[2:3], v[0:1], off
	global_load_dwordx2 v[4:5], v[0:1], off offset:32
	global_load_dwordx2 v[6:7], v[0:1], off offset:64
	global_load_dwordx2 v[8:9], v[0:1], off offset:96
	global_load_dwordx2 v[10:11], v[0:1], off offset:128
	global_load_dwordx2 v[12:13], v[0:1], off offset:160
	global_load_dwordx2 v[14:15], v[0:1], off offset:192
	global_load_dwordx2 v[18:19], v[16:17], off offset:32
	global_load_dwordx2 v[20:21], v[16:17], off offset:64
	global_load_dwordx2 v[22:23], v[16:17], off offset:96
	global_load_dwordx2 v[24:25], v[16:17], off offset:128
	global_load_dwordx2 v[26:27], v[16:17], off offset:160
	global_load_dwordx2 v[30:31], v[16:17], off offset:192
	s_nop 0
	global_load_dwordx2 v[28:29], v[28:29], off
	s_nop 0
	global_load_dwordx2 v[0:1], v[0:1], off offset:224
	s_nop 0
	global_load_dwordx2 v[16:17], v[16:17], off offset:224
	s_lshl_b32 s10, s10, 2
	s_or_b32 s18, s10, s9
	s_mov_b32 s9, s77
	s_ashr_i32 s19, s17, 31
	v_lshl_add_u64 v[94:95], v[46:47], 0, s[8:9]
	v_mov_b64_e32 v[86:87], s[44:45]
	v_mad_i64_i32 v[86:87], s[20:21], v52, s59, v[86:87]
	s_lshl_b32 s76, s8, 1
	v_lshl_add_u64 v[86:87], v[86:87], 0, s[76:77]
	v_lshlrev_b64 v[92:93], 1, v[44:45]
	v_lshl_add_u64 v[86:87], v[86:87], 0, v[92:93]
	s_mov_b64 s[20:21], 0xbcfa800
	v_lshl_add_u64 v[86:87], v[86:87], 0, s[20:21]
	global_load_dwordx2 v[184:185], v[86:87], off
	global_load_dwordx4 v[200:203], v[48:49], off
	global_load_dwordx2 v[186:187], v[86:87], off offset:32
	global_load_dwordx4 v[204:207], v[48:49], off offset:64
	global_load_dwordx2 v[188:189], v[86:87], off offset:64
	global_load_dwordx4 v[208:211], v[48:49], off offset:128
	global_load_dwordx2 v[190:191], v[86:87], off offset:96
	global_load_dwordx4 v[212:215], v[48:49], off offset:192
	global_load_dwordx2 v[192:193], v[86:87], off offset:128
	global_load_dwordx4 v[218:221], v[48:49], off offset:256
	global_load_dwordx2 v[194:195], v[86:87], off offset:160
	global_load_dwordx4 v[222:225], v[48:49], off offset:320
	global_load_dwordx2 v[196:197], v[86:87], off offset:192
	global_load_dwordx4 v[226:229], v[48:49], off offset:384
	global_load_dwordx2 v[198:199], v[86:87], off offset:224
	global_load_dwordx4 v[230:233], v[48:49], off offset:448
	s_add_i32 s9, s18, 0
	s_mul_hi_i32 s21, s9, 36
	s_mul_i32 s9, s9, 36
	s_add_u32 s20, s9, s17
	s_addc_u32 s21, s21, s19
	s_lshl_b64 s[20:21], s[20:21], 16
	v_lshl_add_u64 v[86:87], v[102:103], 0, s[20:21]
	s_movk_i32 s76, 0x1000
	v_lshl_add_u64 v[92:93], v[86:87], 0, s[76:77]
	s_lshl_b32 s100, s66, 7
	s_mov_b32 m0, s100
	s_nop 0
	global_load_lds_dwordx4 v[86:87], off
	global_load_lds_dwordx4 v[86:87], off offset:1024
	global_load_lds_dwordx4 v[86:87], off offset:2048
	global_load_lds_dwordx4 v[86:87], off offset:3072
	s_add_i32 m0, s100, 0x1000
	s_nop 0
	global_load_lds_dwordx4 v[92:93], off
	global_load_lds_dwordx4 v[92:93], off offset:1024
	global_load_lds_dwordx4 v[92:93], off offset:2048
	global_load_lds_dwordx4 v[92:93], off offset:3072
	s_mov_b32 s76, 0x0
	v_lshl_add_u64 v[32:33], s[76:77], 0, v[52:53]
	v_lshlrev_b64 v[32:33], 10, v[32:33]
	v_lshl_add_u64 v[86:87], v[94:95], 0, v[32:33]
	global_load_dwordx4 v[104:107], v[86:87], off
	global_load_dwordx4 v[108:111], v[86:87], off offset:64
	global_load_dwordx4 v[112:115], v[86:87], off offset:128
	global_load_dwordx4 v[116:119], v[86:87], off offset:192
	s_add_i32 s9, s18, 16
	s_mul_hi_i32 s21, s9, 36
	s_mul_i32 s9, s9, 36
	s_add_u32 s20, s9, s17
	s_addc_u32 s21, s21, s19
	s_lshl_b64 s[20:21], s[20:21], 16
	v_lshl_add_u64 v[86:87], v[102:103], 0, s[20:21]
	s_movk_i32 s76, 0x1000
	v_lshl_add_u64 v[92:93], v[86:87], 0, s[76:77]
	s_lshl_b32 s100, s66, 7
	s_add_i32 s100, s100, 0x10000
	s_mov_b32 m0, s100
	s_nop 0
	global_load_lds_dwordx4 v[86:87], off
	global_load_lds_dwordx4 v[86:87], off offset:1024
	global_load_lds_dwordx4 v[86:87], off offset:2048
	global_load_lds_dwordx4 v[86:87], off offset:3072
	s_add_i32 m0, s100, 0x1000
	s_nop 0
	global_load_lds_dwordx4 v[92:93], off
	global_load_lds_dwordx4 v[92:93], off offset:1024
	global_load_lds_dwordx4 v[92:93], off offset:2048
	global_load_lds_dwordx4 v[92:93], off offset:3072
	s_mov_b32 s76, 0x2400
	v_lshl_add_u64 v[32:33], s[76:77], 0, v[52:53]
	v_lshlrev_b64 v[32:33], 10, v[32:33]
	v_lshl_add_u64 v[86:87], v[94:95], 0, v[32:33]
	global_load_dwordx4 v[250:253], v[86:87], off
	global_load_dwordx4 v[82:85], v[86:87], off offset:64
	global_load_dwordx4 v[98:101], v[86:87], off offset:128
	global_load_dwordx4 v[88:91], v[86:87], off offset:192
	s_mov_b32 s9, s77
	s_waitcnt vmcnt(40)
	v_lshlrev_b32_e32 v32, 16, v2
	v_and_b32_e32 v33, 0xffff0000, v2
	v_lshlrev_b32_e32 v34, 16, v3
	v_and_b32_e32 v35, 0xffff0000, v3
	v_lshlrev_b32_e32 v36, 16, v4
	v_and_b32_e32 v37, 0xffff0000, v4
	v_lshlrev_b32_e32 v38, 16, v5
	v_and_b32_e32 v39, 0xffff0000, v5
	v_lshlrev_b32_e32 v40, 16, v6
	v_and_b32_e32 v41, 0xffff0000, v6
	v_lshlrev_b32_e32 v42, 16, v7
	v_and_b32_e32 v43, 0xffff0000, v7
	v_lshlrev_b32_e32 v56, 16, v8
	v_and_b32_e32 v57, 0xffff0000, v8
	v_lshlrev_b32_e32 v58, 16, v9
	v_and_b32_e32 v59, 0xffff0000, v9
	v_lshlrev_b32_e32 v60, 16, v10
	v_and_b32_e32 v61, 0xffff0000, v10
	v_lshlrev_b32_e32 v66, 16, v11
	v_and_b32_e32 v67, 0xffff0000, v11
	v_lshlrev_b32_e32 v8, 16, v12
	v_and_b32_e32 v9, 0xffff0000, v12
	v_lshlrev_b32_e32 v10, 16, v13
	v_and_b32_e32 v11, 0xffff0000, v13
	v_lshlrev_b32_e32 v4, 16, v14
	v_and_b32_e32 v5, 0xffff0000, v14
	v_lshlrev_b32_e32 v6, 16, v15
	v_and_b32_e32 v7, 0xffff0000, v15
	v_lshlrev_b32_e32 v68, 16, v18
	v_and_b32_e32 v69, 0xffff0000, v18
	v_lshlrev_b32_e32 v70, 16, v19
	v_and_b32_e32 v71, 0xffff0000, v19
	v_lshlrev_b32_e32 v72, 16, v20
	v_and_b32_e32 v73, 0xffff0000, v20
	v_lshlrev_b32_e32 v20, 16, v21
	v_and_b32_e32 v21, 0xffff0000, v21
	v_lshlrev_b32_e32 v12, 16, v22
	v_and_b32_e32 v13, 0xffff0000, v22
	v_lshlrev_b32_e32 v14, 16, v23
	v_and_b32_e32 v15, 0xffff0000, v23
	v_lshlrev_b32_e32 v22, 16, v24
	v_and_b32_e32 v23, 0xffff0000, v24
	v_lshlrev_b32_e32 v18, 16, v25
	v_and_b32_e32 v19, 0xffff0000, v25
	v_lshlrev_b32_e32 v24, 16, v26
	v_and_b32_e32 v25, 0xffff0000, v26
	v_lshlrev_b32_e32 v26, 16, v27
	v_and_b32_e32 v27, 0xffff0000, v27
	v_lshlrev_b32_e32 v74, 16, v30
	v_and_b32_e32 v75, 0xffff0000, v30
	v_lshlrev_b32_e32 v30, 16, v31
	v_and_b32_e32 v31, 0xffff0000, v31
	v_lshlrev_b32_e32 v76, 16, v28
	v_and_b32_e32 v77, 0xffff0000, v28
	v_lshlrev_b32_e32 v28, 16, v29
	v_and_b32_e32 v29, 0xffff0000, v29
	v_lshlrev_b32_e32 v78, 16, v0
	v_and_b32_e32 v79, 0xffff0000, v0
	v_lshlrev_b32_e32 v80, 16, v16
	v_and_b32_e32 v81, 0xffff0000, v16
	v_lshlrev_b32_e32 v0, 16, v1
	v_lshlrev_b32_e32 v2, 16, v17
	v_and_b32_e32 v3, 0xffff0000, v17
	v_and_b32_e32 v1, 0xffff0000, v1
	v_pk_add_f32 v[2:3], v[0:1], v[2:3]
	v_pk_add_f32 v[0:1], v[78:79], v[80:81]
	v_pk_add_f32 v[6:7], v[6:7], v[30:31]
	v_pk_add_f32 v[4:5], v[4:5], v[74:75]
	v_pk_add_f32 v[10:11], v[10:11], v[26:27]
	v_pk_add_f32 v[8:9], v[8:9], v[24:25]
	v_pk_add_f32 v[18:19], v[66:67], v[18:19]
	v_pk_add_f32 v[16:17], v[60:61], v[22:23]
	v_pk_add_f32 v[14:15], v[58:59], v[14:15]
	v_pk_add_f32 v[12:13], v[56:57], v[12:13]
	v_pk_add_f32 v[22:23], v[42:43], v[20:21]
	v_pk_add_f32 v[20:21], v[40:41], v[72:73]
	v_pk_add_f32 v[26:27], v[38:39], v[70:71]
	v_pk_add_f32 v[24:25], v[36:37], v[68:69]
	v_pk_add_f32 v[30:31], v[34:35], v[28:29]
	v_pk_add_f32 v[28:29], v[32:33], v[76:77]
	s_waitcnt vmcnt(12)
	s_barrier
	ds_read_b128 v[120:123], v65
	ds_read_b128 v[124:127], v65 offset:4096
	ds_read_b128 v[128:131], v65 offset:8192
	ds_read_b128 v[132:135], v65 offset:12288
	ds_read_b128 v[136:139], v65 offset:16384
	ds_read_b128 v[140:143], v65 offset:20480
	ds_read_b128 v[144:147], v65 offset:24576
	ds_read_b128 v[148:151], v65 offset:28672
	ds_read_b128 v[152:155], v65 offset:1024
	ds_read_b128 v[156:159], v65 offset:5120
	ds_read_b128 v[160:163], v65 offset:9216
	ds_read_b128 v[164:167], v65 offset:13312
	ds_read_b128 v[168:171], v65 offset:17408
	ds_read_b128 v[172:175], v65 offset:21504
	ds_read_b128 v[176:179], v65 offset:25600
	ds_read_b128 v[180:183], v65 offset:29696
	s_waitcnt lgkmcnt(8)
	v_mfma_f32_16x16x32_bf16 v[28:31], v[120:123], v[104:107], v[28:31]
	v_mfma_f32_16x16x32_bf16 v[24:27], v[124:127], v[104:107], v[24:27]
	v_mfma_f32_16x16x32_bf16 v[20:23], v[128:131], v[104:107], v[20:23]
	v_mfma_f32_16x16x32_bf16 v[12:15], v[132:135], v[104:107], v[12:15]
	v_mfma_f32_16x16x32_bf16 v[16:19], v[136:139], v[104:107], v[16:19]
	v_mfma_f32_16x16x32_bf16 v[8:11], v[140:143], v[104:107], v[8:11]
	v_mfma_f32_16x16x32_bf16 v[4:7], v[144:147], v[104:107], v[4:7]
	v_mfma_f32_16x16x32_bf16 v[0:3], v[148:151], v[104:107], v[0:3]
	ds_read_b128 v[120:123], v65 offset:2048
	ds_read_b128 v[124:127], v65 offset:6144
	ds_read_b128 v[128:131], v65 offset:10240
	ds_read_b128 v[132:135], v65 offset:14336
	ds_read_b128 v[136:139], v65 offset:18432
	ds_read_b128 v[140:143], v65 offset:22528
	ds_read_b128 v[144:147], v65 offset:26624
	ds_read_b128 v[148:151], v65 offset:30720
	s_waitcnt lgkmcnt(8)
	v_mfma_f32_16x16x32_bf16 v[28:31], v[152:155], v[108:111], v[28:31]
	v_mfma_f32_16x16x32_bf16 v[24:27], v[156:159], v[108:111], v[24:27]
	v_mfma_f32_16x16x32_bf16 v[20:23], v[160:163], v[108:111], v[20:23]
	v_mfma_f32_16x16x32_bf16 v[12:15], v[164:167], v[108:111], v[12:15]
	v_mfma_f32_16x16x32_bf16 v[16:19], v[168:171], v[108:111], v[16:19]
	v_mfma_f32_16x16x32_bf16 v[8:11], v[172:175], v[108:111], v[8:11]
	v_mfma_f32_16x16x32_bf16 v[4:7], v[176:179], v[108:111], v[4:7]
	v_mfma_f32_16x16x32_bf16 v[0:3], v[180:183], v[108:111], v[0:3]
	ds_read_b128 v[152:155], v65 offset:3072
	ds_read_b128 v[156:159], v65 offset:7168
	ds_read_b128 v[160:163], v65 offset:11264
	ds_read_b128 v[164:167], v65 offset:15360
	ds_read_b128 v[168:171], v65 offset:19456
	ds_read_b128 v[172:175], v65 offset:23552
	ds_read_b128 v[176:179], v65 offset:27648
	ds_read_b128 v[180:183], v65 offset:31744
	s_waitcnt lgkmcnt(8)
	v_mfma_f32_16x16x32_bf16 v[28:31], v[120:123], v[112:115], v[28:31]
	v_mfma_f32_16x16x32_bf16 v[24:27], v[124:127], v[112:115], v[24:27]
	v_mfma_f32_16x16x32_bf16 v[20:23], v[128:131], v[112:115], v[20:23]
	v_mfma_f32_16x16x32_bf16 v[12:15], v[132:135], v[112:115], v[12:15]
	v_mfma_f32_16x16x32_bf16 v[16:19], v[136:139], v[112:115], v[16:19]
	v_mfma_f32_16x16x32_bf16 v[8:11], v[140:143], v[112:115], v[8:11]
	v_mfma_f32_16x16x32_bf16 v[4:7], v[144:147], v[112:115], v[4:7]
	v_mfma_f32_16x16x32_bf16 v[0:3], v[148:151], v[112:115], v[0:3]
	s_waitcnt lgkmcnt(0)
	v_mfma_f32_16x16x32_bf16 v[28:31], v[152:155], v[116:119], v[28:31]
	v_mfma_f32_16x16x32_bf16 v[24:27], v[156:159], v[116:119], v[24:27]
	v_mfma_f32_16x16x32_bf16 v[20:23], v[160:163], v[116:119], v[20:23]
	v_mfma_f32_16x16x32_bf16 v[12:15], v[164:167], v[116:119], v[12:15]
	v_mfma_f32_16x16x32_bf16 v[16:19], v[168:171], v[116:119], v[16:19]
	v_mfma_f32_16x16x32_bf16 v[8:11], v[172:175], v[116:119], v[8:11]
	v_mfma_f32_16x16x32_bf16 v[4:7], v[176:179], v[116:119], v[4:7]
	v_mfma_f32_16x16x32_bf16 v[0:3], v[180:183], v[116:119], v[0:3]
	s_waitcnt vmcnt(0)
	s_barrier
	v_add_u32_e32 v94, 0x10000, v65
	ds_read_b128 v[120:123], v94
	ds_read_b128 v[124:127], v94 offset:4096
	ds_read_b128 v[128:131], v94 offset:8192
	ds_read_b128 v[132:135], v94 offset:12288
	ds_read_b128 v[136:139], v94 offset:16384
	ds_read_b128 v[140:143], v94 offset:20480
	ds_read_b128 v[144:147], v94 offset:24576
	ds_read_b128 v[148:151], v94 offset:28672
	ds_read_b128 v[152:155], v94 offset:1024
	ds_read_b128 v[156:159], v94 offset:5120
	ds_read_b128 v[160:163], v94 offset:9216
	ds_read_b128 v[164:167], v94 offset:13312
	ds_read_b128 v[168:171], v94 offset:17408
	ds_read_b128 v[172:175], v94 offset:21504
	ds_read_b128 v[176:179], v94 offset:25600
	ds_read_b128 v[180:183], v94 offset:29696
	s_waitcnt lgkmcnt(8)
	v_mfma_f32_16x16x32_bf16 v[28:31], v[120:123], v[250:253], v[28:31]
	v_mfma_f32_16x16x32_bf16 v[24:27], v[124:127], v[250:253], v[24:27]
	v_mfma_f32_16x16x32_bf16 v[20:23], v[128:131], v[250:253], v[20:23]
	v_mfma_f32_16x16x32_bf16 v[12:15], v[132:135], v[250:253], v[12:15]
	v_mfma_f32_16x16x32_bf16 v[16:19], v[136:139], v[250:253], v[16:19]
	v_mfma_f32_16x16x32_bf16 v[8:11], v[140:143], v[250:253], v[8:11]
	v_mfma_f32_16x16x32_bf16 v[4:7], v[144:147], v[250:253], v[4:7]
	v_mfma_f32_16x16x32_bf16 v[0:3], v[148:151], v[250:253], v[0:3]
	ds_read_b128 v[120:123], v94 offset:2048
	ds_read_b128 v[124:127], v94 offset:6144
	ds_read_b128 v[128:131], v94 offset:10240
	ds_read_b128 v[132:135], v94 offset:14336
	ds_read_b128 v[136:139], v94 offset:18432
	ds_read_b128 v[140:143], v94 offset:22528
	ds_read_b128 v[144:147], v94 offset:26624
	ds_read_b128 v[148:151], v94 offset:30720
	s_waitcnt lgkmcnt(8)
	v_mfma_f32_16x16x32_bf16 v[28:31], v[152:155], v[82:85], v[28:31]
	v_mfma_f32_16x16x32_bf16 v[24:27], v[156:159], v[82:85], v[24:27]
	v_mfma_f32_16x16x32_bf16 v[20:23], v[160:163], v[82:85], v[20:23]
	v_mfma_f32_16x16x32_bf16 v[12:15], v[164:167], v[82:85], v[12:15]
	v_mfma_f32_16x16x32_bf16 v[16:19], v[168:171], v[82:85], v[16:19]
	v_mfma_f32_16x16x32_bf16 v[8:11], v[172:175], v[82:85], v[8:11]
	v_mfma_f32_16x16x32_bf16 v[4:7], v[176:179], v[82:85], v[4:7]
	v_mfma_f32_16x16x32_bf16 v[0:3], v[180:183], v[82:85], v[0:3]
	ds_read_b128 v[152:155], v94 offset:3072
	ds_read_b128 v[156:159], v94 offset:7168
	ds_read_b128 v[160:163], v94 offset:11264
	ds_read_b128 v[164:167], v94 offset:15360
	ds_read_b128 v[168:171], v94 offset:19456
	ds_read_b128 v[172:175], v94 offset:23552
	ds_read_b128 v[176:179], v94 offset:27648
	ds_read_b128 v[180:183], v94 offset:31744
	s_waitcnt lgkmcnt(8)
	v_mfma_f32_16x16x32_bf16 v[28:31], v[120:123], v[98:101], v[28:31]
	v_mfma_f32_16x16x32_bf16 v[24:27], v[124:127], v[98:101], v[24:27]
	v_mfma_f32_16x16x32_bf16 v[20:23], v[128:131], v[98:101], v[20:23]
	v_mfma_f32_16x16x32_bf16 v[12:15], v[132:135], v[98:101], v[12:15]
	v_mfma_f32_16x16x32_bf16 v[16:19], v[136:139], v[98:101], v[16:19]
	v_mfma_f32_16x16x32_bf16 v[8:11], v[140:143], v[98:101], v[8:11]
	v_mfma_f32_16x16x32_bf16 v[4:7], v[144:147], v[98:101], v[4:7]
	v_mfma_f32_16x16x32_bf16 v[0:3], v[148:151], v[98:101], v[0:3]
	s_waitcnt lgkmcnt(0)
	v_mfma_f32_16x16x32_bf16 v[28:31], v[152:155], v[88:91], v[28:31]
	v_mfma_f32_16x16x32_bf16 v[24:27], v[156:159], v[88:91], v[24:27]
	v_mfma_f32_16x16x32_bf16 v[20:23], v[160:163], v[88:91], v[20:23]
	v_mfma_f32_16x16x32_bf16 v[12:15], v[164:167], v[88:91], v[12:15]
	v_mfma_f32_16x16x32_bf16 v[16:19], v[168:171], v[88:91], v[16:19]
	v_mfma_f32_16x16x32_bf16 v[8:11], v[172:175], v[88:91], v[8:11]
	v_mfma_f32_16x16x32_bf16 v[4:7], v[176:179], v[88:91], v[4:7]
	v_mfma_f32_16x16x32_bf16 v[0:3], v[180:183], v[88:91], v[0:3]
	s_nop 1
	v_mul_f32_e32 v32, v29, v29
	v_mul_f32_e32 v33, v25, v25
	v_fmac_f32_e32 v32, v28, v28
	v_fmac_f32_e32 v33, v24, v24
	v_fmac_f32_e32 v32, v30, v30
	v_fmac_f32_e32 v33, v26, v26
	v_fmac_f32_e32 v32, v31, v31
	v_fmac_f32_e32 v33, v27, v27
	v_add_f32_e32 v32, v32, v33
	v_mul_f32_e32 v33, v21, v21
	v_fmac_f32_e32 v33, v20, v20
	v_fmac_f32_e32 v33, v22, v22
	v_fmac_f32_e32 v33, v23, v23
	v_add_f32_e32 v32, v32, v33
	v_mul_f32_e32 v33, v13, v13
	v_fmac_f32_e32 v33, v12, v12
	v_fmac_f32_e32 v33, v14, v14
	v_fmac_f32_e32 v33, v15, v15
	v_add_f32_e32 v32, v32, v33
	v_mul_f32_e32 v33, v17, v17
	v_fmac_f32_e32 v33, v16, v16
	v_fmac_f32_e32 v33, v18, v18
	v_fmac_f32_e32 v33, v19, v19
	v_add_f32_e32 v32, v32, v33
	v_mul_f32_e32 v33, v9, v9
	v_fmac_f32_e32 v33, v8, v8
	v_fmac_f32_e32 v33, v10, v10
	v_fmac_f32_e32 v33, v11, v11
	v_add_f32_e32 v32, v32, v33
	v_mul_f32_e32 v33, v5, v5
	v_fmac_f32_e32 v33, v4, v4
	v_fmac_f32_e32 v33, v6, v6
	v_fmac_f32_e32 v33, v7, v7
	v_add_f32_e32 v32, v32, v33
	v_mul_f32_e32 v33, v1, v1
	v_fmac_f32_e32 v33, v0, v0
	v_fmac_f32_e32 v33, v2, v2
	v_fmac_f32_e32 v33, v3, v3
	v_add_f32_e32 v32, v32, v33
	ds_swizzle_b32 v33, v32 offset:swizzle(SWAP,16)
	s_waitcnt lgkmcnt(0)
	s_barrier
	v_add_f32_e32 v32, v32, v33
	v_mov_b32_e32 v33, v32
	s_nop 1
	v_permlane32_swap_b32_e32 v32, v33
	s_and_saveexec_b64 s[10:11], s[2:3]
	s_cbranch_execz .LBB0_1053
	v_add_f32_e32 v32, v32, v33
	ds_write_b32 v64, v32
	s_branch .LBB0_1053
